# combo10c + strategy 7 (instruction selection): per-unit accumulator zeroing with 64 v_mov_b64 instead of 128 v_mov_b32 in all five GEMM phases
# speedup vs baseline: 1.0025x; 1.0025x over previous
.LBB0_199:
	s_ashr_i32 s31, s30, 31
	s_lshl_b64 s[36:37], s[30:31], 20
	s_add_u32 s36, s0, s36
	s_addc_u32 s37, s1, s37
	s_and_b64 s[40:41], s[6:7], exec
	s_cselect_b32 s31, s37, s43
	s_cselect_b32 s35, s36, s42
	s_ashr_i32 s29, s28, 31
	s_lshl_b64 s[40:41], s[28:29], 20
	s_add_u32 s40, s2, s40
	s_addc_u32 s41, s3, s41
	s_and_b64 s[46:47], s[6:7], exec
	s_cselect_b32 s29, s41, s45
	s_cselect_b32 s39, s40, s44
	s_add_u32 s42, s42, 0x80080
	s_addc_u32 s43, s43, 0
	s_add_u32 s66, s44, 0x100
	v_mov_b64_e32 v[32:33], 0
	s_addc_u32 s67, s45, 0
	s_mov_b32 s68, -2
	v_mov_b64_e32 v[34:35], 0
	v_mov_b64_e32 v[36:37], 0
	v_mov_b64_e32 v[38:39], 0
	v_mov_b64_e32 v[40:41], 0
	v_mov_b64_e32 v[42:43], 0
	v_mov_b64_e32 v[44:45], 0
	v_mov_b64_e32 v[46:47], 0
	v_mov_b64_e32 v[48:49], 0
	v_mov_b64_e32 v[50:51], 0
	v_mov_b64_e32 v[52:53], 0
	v_mov_b64_e32 v[54:55], 0
	v_mov_b64_e32 v[56:57], 0
	v_mov_b64_e32 v[58:59], 0
	v_mov_b64_e32 v[60:61], 0
	v_mov_b64_e32 v[62:63], 0
	v_mov_b64_e32 v[64:65], 0
	v_mov_b64_e32 v[66:67], 0
	v_mov_b64_e32 v[68:69], 0
	v_mov_b64_e32 v[70:71], 0
	v_mov_b64_e32 v[72:73], 0
	v_mov_b64_e32 v[74:75], 0
	v_mov_b64_e32 v[76:77], 0
	v_mov_b64_e32 v[78:79], 0
	v_mov_b64_e32 v[80:81], 0
	v_mov_b64_e32 v[82:83], 0
	v_mov_b64_e32 v[84:85], 0
	v_mov_b64_e32 v[86:87], 0
	v_mov_b64_e32 v[88:89], 0
	v_mov_b64_e32 v[90:91], 0
	v_mov_b64_e32 v[92:93], 0
	v_mov_b64_e32 v[94:95], 0
	v_mov_b64_e32 v[96:97], 0
	v_mov_b64_e32 v[98:99], 0
	v_mov_b64_e32 v[100:101], 0
	v_mov_b64_e32 v[102:103], 0
	v_mov_b64_e32 v[104:105], 0
	v_mov_b64_e32 v[106:107], 0
	v_mov_b64_e32 v[108:109], 0
	v_mov_b64_e32 v[110:111], 0
	v_mov_b64_e32 v[112:113], 0
	v_mov_b64_e32 v[114:115], 0
	v_mov_b64_e32 v[116:117], 0
	v_mov_b64_e32 v[118:119], 0
	v_mov_b64_e32 v[120:121], 0
	v_mov_b64_e32 v[122:123], 0
	v_mov_b64_e32 v[124:125], 0
	v_mov_b64_e32 v[126:127], 0
	v_mov_b64_e32 v[128:129], 0
	v_mov_b64_e32 v[130:131], 0
	v_mov_b64_e32 v[132:133], 0
	v_mov_b64_e32 v[134:135], 0
	v_mov_b64_e32 v[136:137], 0
	v_mov_b64_e32 v[138:139], 0
	v_mov_b64_e32 v[140:141], 0
	v_mov_b64_e32 v[142:143], 0
	v_mov_b64_e32 v[144:145], 0
	v_mov_b64_e32 v[146:147], 0
	v_mov_b64_e32 v[148:149], 0
	v_mov_b64_e32 v[150:151], 0
	v_mov_b64_e32 v[152:153], 0
	v_mov_b64_e32 v[154:155], 0
	v_mov_b64_e32 v[156:157], 0
	v_mov_b64_e32 v[158:159], 0

.LBB0_561:
	s_ashr_i32 s23, s22, 31
	s_lshl_b64 s[24:25], s[22:23], 20
	s_add_u32 s24, s1, s24
	s_addc_u32 s25, s2, s25
	s_and_b64 s[26:27], s[4:5], exec
	s_cselect_b32 s23, s25, s31
	s_cselect_b32 s55, s24, s30
	s_ashr_i32 s21, s20, 31
	s_lshl_b64 s[26:27], s[20:21], 20
	s_add_u32 s26, s3, s26
	s_addc_u32 s27, s19, s27
	s_and_b64 s[36:37], s[4:5], exec
	s_cselect_b32 s21, s27, s35
	s_cselect_b32 s56, s26, s34
	s_add_u32 s30, s30, 0x80080
	s_addc_u32 s31, s31, 0
	s_add_u32 s57, s34, 0x100
	v_mov_b64_e32 v[32:33], 0
	s_addc_u32 s58, s35, 0
	s_mov_b32 s59, -2
	v_mov_b64_e32 v[34:35], 0
	v_mov_b64_e32 v[36:37], 0
	v_mov_b64_e32 v[38:39], 0
	v_mov_b64_e32 v[40:41], 0
	v_mov_b64_e32 v[42:43], 0
	v_mov_b64_e32 v[44:45], 0
	v_mov_b64_e32 v[46:47], 0
	v_mov_b64_e32 v[64:65], 0
	v_mov_b64_e32 v[66:67], 0
	v_mov_b64_e32 v[68:69], 0
	v_mov_b64_e32 v[70:71], 0
	v_mov_b64_e32 v[72:73], 0
	v_mov_b64_e32 v[74:75], 0
	v_mov_b64_e32 v[76:77], 0
	v_mov_b64_e32 v[78:79], 0
	v_mov_b64_e32 v[48:49], 0
	v_mov_b64_e32 v[50:51], 0
	v_mov_b64_e32 v[52:53], 0
	v_mov_b64_e32 v[54:55], 0
	v_mov_b64_e32 v[56:57], 0
	v_mov_b64_e32 v[58:59], 0
	v_mov_b64_e32 v[60:61], 0
	v_mov_b64_e32 v[62:63], 0
	v_mov_b64_e32 v[80:81], 0
	v_mov_b64_e32 v[82:83], 0
	v_mov_b64_e32 v[84:85], 0
	v_mov_b64_e32 v[86:87], 0
	v_mov_b64_e32 v[88:89], 0
	v_mov_b64_e32 v[90:91], 0
	v_mov_b64_e32 v[92:93], 0
	v_mov_b64_e32 v[94:95], 0
	v_mov_b64_e32 v[96:97], 0
	v_mov_b64_e32 v[98:99], 0
	v_mov_b64_e32 v[100:101], 0
	v_mov_b64_e32 v[102:103], 0
	v_mov_b64_e32 v[104:105], 0
	v_mov_b64_e32 v[106:107], 0
	v_mov_b64_e32 v[108:109], 0
	v_mov_b64_e32 v[110:111], 0
	v_mov_b64_e32 v[128:129], 0
	v_mov_b64_e32 v[130:131], 0
	v_mov_b64_e32 v[132:133], 0
	v_mov_b64_e32 v[134:135], 0
	v_mov_b64_e32 v[136:137], 0
	v_mov_b64_e32 v[138:139], 0
	v_mov_b64_e32 v[140:141], 0
	v_mov_b64_e32 v[142:143], 0
	v_mov_b64_e32 v[112:113], 0
	v_mov_b64_e32 v[114:115], 0
	v_mov_b64_e32 v[116:117], 0
	v_mov_b64_e32 v[118:119], 0
	v_mov_b64_e32 v[120:121], 0
	v_mov_b64_e32 v[122:123], 0
	v_mov_b64_e32 v[124:125], 0
	v_mov_b64_e32 v[126:127], 0
	v_mov_b64_e32 v[144:145], 0
	v_mov_b64_e32 v[146:147], 0
	v_mov_b64_e32 v[148:149], 0
	v_mov_b64_e32 v[150:151], 0
	v_mov_b64_e32 v[152:153], 0
	v_mov_b64_e32 v[154:155], 0
	v_mov_b64_e32 v[156:157], 0
	v_mov_b64_e32 v[158:159], 0

.LBB0_686:
	s_ashr_i32 s19, s18, 31
	s_lshl_b64 s[20:21], s[18:19], 21
	s_add_u32 s20, s0, s20
	s_addc_u32 s21, s1, s21
	s_and_b64 s[22:23], s[4:5], exec
	s_cselect_b32 s19, s21, s25
	s_cselect_b32 s50, s20, s24
	s_ashr_i32 s17, s16, 31
	s_lshl_b64 s[22:23], s[16:17], 21
	s_add_u32 s22, s3, s22
	s_addc_u32 s23, s30, s23
	s_and_b64 s[28:29], s[4:5], exec
	s_cselect_b32 s17, s23, s27
	s_cselect_b32 s51, s22, s26
	s_add_u32 s24, s24, 0x100080
	s_addc_u32 s25, s25, 0
	s_add_u32 s52, s26, 0x100
	v_mov_b64_e32 v[0:1], 0
	s_addc_u32 s53, s27, 0
	s_mov_b32 s54, -2
	v_mov_b64_e32 v[2:3], 0
	v_mov_b64_e32 v[4:5], 0
	v_mov_b64_e32 v[6:7], 0
	v_mov_b64_e32 v[8:9], 0
	v_mov_b64_e32 v[10:11], 0
	v_mov_b64_e32 v[12:13], 0
	v_mov_b64_e32 v[14:15], 0
	v_mov_b64_e32 v[16:17], 0
	v_mov_b64_e32 v[18:19], 0
	v_mov_b64_e32 v[20:21], 0
	v_mov_b64_e32 v[22:23], 0
	v_mov_b64_e32 v[24:25], 0
	v_mov_b64_e32 v[26:27], 0
	v_mov_b64_e32 v[28:29], 0
	v_mov_b64_e32 v[30:31], 0
	v_mov_b64_e32 v[32:33], 0
	v_mov_b64_e32 v[34:35], 0
	v_mov_b64_e32 v[36:37], 0
	v_mov_b64_e32 v[38:39], 0
	v_mov_b64_e32 v[40:41], 0
	v_mov_b64_e32 v[42:43], 0
	v_mov_b64_e32 v[44:45], 0
	v_mov_b64_e32 v[46:47], 0
	v_mov_b64_e32 v[48:49], 0
	v_mov_b64_e32 v[50:51], 0
	v_mov_b64_e32 v[52:53], 0
	v_mov_b64_e32 v[54:55], 0
	v_mov_b64_e32 v[56:57], 0
	v_mov_b64_e32 v[58:59], 0
	v_mov_b64_e32 v[60:61], 0
	v_mov_b64_e32 v[62:63], 0
	v_mov_b64_e32 v[64:65], 0
	v_mov_b64_e32 v[66:67], 0
	v_mov_b64_e32 v[68:69], 0
	v_mov_b64_e32 v[70:71], 0
	v_mov_b64_e32 v[72:73], 0
	v_mov_b64_e32 v[74:75], 0
	v_mov_b64_e32 v[76:77], 0
	v_mov_b64_e32 v[78:79], 0
	v_mov_b64_e32 v[80:81], 0
	v_mov_b64_e32 v[82:83], 0
	v_mov_b64_e32 v[84:85], 0
	v_mov_b64_e32 v[86:87], 0
	v_mov_b64_e32 v[88:89], 0
	v_mov_b64_e32 v[90:91], 0
	v_mov_b64_e32 v[92:93], 0
	v_mov_b64_e32 v[94:95], 0
	v_mov_b64_e32 v[96:97], 0
	v_mov_b64_e32 v[98:99], 0
	v_mov_b64_e32 v[100:101], 0
	v_mov_b64_e32 v[102:103], 0
	v_mov_b64_e32 v[104:105], 0
	v_mov_b64_e32 v[106:107], 0
	v_mov_b64_e32 v[108:109], 0
	v_mov_b64_e32 v[110:111], 0
	v_mov_b64_e32 v[112:113], 0
	v_mov_b64_e32 v[114:115], 0
	v_mov_b64_e32 v[116:117], 0
	v_mov_b64_e32 v[118:119], 0
	v_mov_b64_e32 v[120:121], 0
	v_mov_b64_e32 v[122:123], 0
	v_mov_b64_e32 v[124:125], 0
	v_mov_b64_e32 v[126:127], 0

.LBB0_939:
	s_ashr_i32 s27, s26, 31
	s_lshl_b64 s[28:29], s[26:27], 20
	s_add_u32 s28, s0, s28
	s_addc_u32 s29, s1, s29
	s_and_b64 s[30:31], s[4:5], exec
	s_cselect_b32 s27, s29, s39
	s_cselect_b32 s35, s28, s38
	s_ashr_i32 s25, s24, 31
	s_lshl_b64 s[30:31], s[24:25], 20
	s_add_u32 s30, s2, s30
	s_addc_u32 s31, s3, s31
	s_and_b64 s[42:43], s[4:5], exec
	s_cselect_b32 s25, s31, s41
	s_cselect_b32 s37, s30, s40
	s_add_u32 s38, s38, 0x80080
	s_addc_u32 s39, s39, 0
	s_add_u32 s60, s40, 0x100
	v_mov_b64_e32 v[32:33], 0
	s_mov_b32 s66, s64
	s_addc_u32 s61, s41, 0
	s_mov_b32 s64, -2
	v_mov_b64_e32 v[34:35], 0
	v_mov_b64_e32 v[36:37], 0
	v_mov_b64_e32 v[38:39], 0
	v_mov_b64_e32 v[48:49], 0
	v_mov_b64_e32 v[50:51], 0
	v_mov_b64_e32 v[52:53], 0
	v_mov_b64_e32 v[54:55], 0
	v_mov_b64_e32 v[64:65], 0
	v_mov_b64_e32 v[66:67], 0
	v_mov_b64_e32 v[68:69], 0
	v_mov_b64_e32 v[70:71], 0
	v_mov_b64_e32 v[80:81], 0
	v_mov_b64_e32 v[82:83], 0
	v_mov_b64_e32 v[84:85], 0
	v_mov_b64_e32 v[86:87], 0
	v_mov_b64_e32 v[40:41], 0
	v_mov_b64_e32 v[42:43], 0
	v_mov_b64_e32 v[44:45], 0
	v_mov_b64_e32 v[46:47], 0
	v_mov_b64_e32 v[56:57], 0
	v_mov_b64_e32 v[58:59], 0
	v_mov_b64_e32 v[60:61], 0
	v_mov_b64_e32 v[62:63], 0
	v_mov_b64_e32 v[72:73], 0
	v_mov_b64_e32 v[74:75], 0
	v_mov_b64_e32 v[76:77], 0
	v_mov_b64_e32 v[78:79], 0
	v_mov_b64_e32 v[88:89], 0
	v_mov_b64_e32 v[90:91], 0
	v_mov_b64_e32 v[92:93], 0
	v_mov_b64_e32 v[94:95], 0
	v_mov_b64_e32 v[96:97], 0
	v_mov_b64_e32 v[98:99], 0
	v_mov_b64_e32 v[100:101], 0
	v_mov_b64_e32 v[102:103], 0
	v_mov_b64_e32 v[112:113], 0
	v_mov_b64_e32 v[114:115], 0
	v_mov_b64_e32 v[116:117], 0
	v_mov_b64_e32 v[118:119], 0
	v_mov_b64_e32 v[128:129], 0
	v_mov_b64_e32 v[130:131], 0
	v_mov_b64_e32 v[132:133], 0
	v_mov_b64_e32 v[134:135], 0
	v_mov_b64_e32 v[144:145], 0
	v_mov_b64_e32 v[146:147], 0
	v_mov_b64_e32 v[148:149], 0
	v_mov_b64_e32 v[150:151], 0
	v_mov_b64_e32 v[104:105], 0
	v_mov_b64_e32 v[106:107], 0
	v_mov_b64_e32 v[108:109], 0
	v_mov_b64_e32 v[110:111], 0
	v_mov_b64_e32 v[120:121], 0
	v_mov_b64_e32 v[122:123], 0
	v_mov_b64_e32 v[124:125], 0
	v_mov_b64_e32 v[126:127], 0
	v_mov_b64_e32 v[136:137], 0
	v_mov_b64_e32 v[138:139], 0
	v_mov_b64_e32 v[140:141], 0
	v_mov_b64_e32 v[142:143], 0
	v_mov_b64_e32 v[152:153], 0
	v_mov_b64_e32 v[154:155], 0
	v_mov_b64_e32 v[156:157], 0
	v_mov_b64_e32 v[158:159], 0

.LBB0_1357:
	s_ashr_i32 s19, s18, 31
	s_lshl_b64 s[20:21], s[18:19], 22
	v_readlane_b32 s22, v254, 14
	v_readlane_b32 s23, v254, 15
	s_add_u32 s20, s22, s20
	s_addc_u32 s21, s23, s21
	s_and_b64 s[22:23], s[0:1], exec
	s_cselect_b32 s19, s21, s27
	s_cselect_b32 s55, s20, s26
	s_ashr_i32 s17, s16, 31
	s_lshl_b64 s[22:23], s[16:17], 22
	s_add_u32 s22, s3, s22
	s_addc_u32 s23, s15, s23
	s_and_b64 s[30:31], s[0:1], exec
	s_cselect_b32 s17, s23, s29
	s_cselect_b32 s56, s22, s28
	s_add_u32 s57, s28, 0x100
	v_mov_b64_e32 v[32:33], 0
	s_addc_u32 s58, s29, 0
	s_mov_b32 s59, -2
	v_mov_b64_e32 v[34:35], 0
	v_mov_b64_e32 v[36:37], 0
	v_mov_b64_e32 v[38:39], 0
	v_mov_b64_e32 v[44:45], 0
	v_mov_b64_e32 v[46:47], 0
	v_mov_b64_e32 v[52:53], 0
	v_mov_b64_e32 v[54:55], 0
	v_mov_b64_e32 v[60:61], 0
	v_mov_b64_e32 v[62:63], 0
	v_mov_b64_e32 v[68:69], 0
	v_mov_b64_e32 v[70:71], 0
	v_mov_b64_e32 v[76:77], 0
	v_mov_b64_e32 v[78:79], 0
	v_mov_b64_e32 v[84:85], 0
	v_mov_b64_e32 v[86:87], 0
	v_mov_b64_e32 v[40:41], 0
	v_mov_b64_e32 v[42:43], 0
	v_mov_b64_e32 v[48:49], 0
	v_mov_b64_e32 v[50:51], 0
	v_mov_b64_e32 v[56:57], 0
	v_mov_b64_e32 v[58:59], 0
	v_mov_b64_e32 v[64:65], 0
	v_mov_b64_e32 v[66:67], 0
	v_mov_b64_e32 v[72:73], 0
	v_mov_b64_e32 v[74:75], 0
	v_mov_b64_e32 v[80:81], 0
	v_mov_b64_e32 v[82:83], 0
	v_mov_b64_e32 v[88:89], 0
	v_mov_b64_e32 v[90:91], 0
	v_mov_b64_e32 v[92:93], 0
	v_mov_b64_e32 v[94:95], 0
	v_mov_b64_e32 v[96:97], 0
	v_mov_b64_e32 v[98:99], 0
	v_mov_b64_e32 v[100:101], 0
	v_mov_b64_e32 v[102:103], 0
	v_mov_b64_e32 v[108:109], 0
	v_mov_b64_e32 v[110:111], 0
	v_mov_b64_e32 v[116:117], 0
	v_mov_b64_e32 v[118:119], 0
	v_mov_b64_e32 v[128:129], 0
	v_mov_b64_e32 v[130:131], 0
	v_mov_b64_e32 v[132:133], 0
	v_mov_b64_e32 v[134:135], 0
	v_mov_b64_e32 v[140:141], 0
	v_mov_b64_e32 v[142:143], 0
	v_mov_b64_e32 v[148:149], 0
	v_mov_b64_e32 v[150:151], 0
	v_mov_b64_e32 v[104:105], 0
	v_mov_b64_e32 v[106:107], 0
	v_mov_b64_e32 v[112:113], 0
	v_mov_b64_e32 v[114:115], 0
	v_mov_b64_e32 v[120:121], 0
	v_mov_b64_e32 v[122:123], 0
	v_mov_b64_e32 v[124:125], 0
	v_mov_b64_e32 v[126:127], 0
	v_mov_b64_e32 v[136:137], 0
	v_mov_b64_e32 v[138:139], 0
	v_mov_b64_e32 v[144:145], 0
	v_mov_b64_e32 v[146:147], 0
	v_mov_b64_e32 v[152:153], 0
	v_mov_b64_e32 v[154:155], 0
	v_mov_b64_e32 v[156:157], 0
	v_mov_b64_e32 v[158:159], 0
